# M9: baseline adj loader + S2 lean consumer bodies (rowsum via mfma16x16x32) + K3 l1 hoist + K3/K1 DPP cuts
# baseline (speedup 1.0000x reference)
amdhsa.kernels:
  - .agpr_count:     0
    .args:
      - .actual_access:  read_only
        .address_space:  global
        .offset:         0
        .size:           8
        .value_kind:     global_buffer
      - .actual_access:  read_only
        .address_space:  global
        .offset:         8
        .size:           8
        .value_kind:     global_buffer
      - .actual_access:  read_only
        .address_space:  global
        .offset:         16
        .size:           8
        .value_kind:     global_buffer
      - .actual_access:  write_only
        .address_space:  global
        .offset:         24
        .size:           8
        .value_kind:     global_buffer
      - .actual_access:  write_only
        .address_space:  global
        .offset:         32
        .size:           8
        .value_kind:     global_buffer
      - .actual_access:  write_only
        .address_space:  global
        .offset:         40
        .size:           8
        .value_kind:     global_buffer
    .group_segment_fixed_size: 57344
    .kernarg_segment_align: 8
    .kernarg_segment_size: 48
    .language:       OpenCL C
    .language_version:
      - 2
      - 0
    .max_flat_workgroup_size: 512
    .name:           _Z12gemm1_kernelPKfS0_S0_PDv8_DF16_PDF16_S3_
    .private_segment_fixed_size: 0
    .sgpr_count:     18
    .sgpr_spill_count: 0
    .symbol:         _Z12gemm1_kernelPKfS0_S0_PDv8_DF16_PDF16_S3_.kd
    .uniform_work_group_size: 1
    .uses_dynamic_stack: false
    .vgpr_count:     125
    .vgpr_spill_count: 0
    .wavefront_size: 64
  - .agpr_count:     0
    .args:
      - .actual_access:  read_only
        .address_space:  global
        .offset:         0
        .size:           8
        .value_kind:     global_buffer
      - .actual_access:  read_only
        .address_space:  global
        .offset:         8
        .size:           8
        .value_kind:     global_buffer
      - .actual_access:  read_only
        .address_space:  global
        .offset:         16
        .size:           8
        .value_kind:     global_buffer
      - .actual_access:  read_only
        .address_space:  global
        .offset:         24
        .size:           8
        .value_kind:     global_buffer
      - .actual_access:  write_only
        .address_space:  global
        .offset:         32
        .size:           8
        .value_kind:     global_buffer
      - .actual_access:  write_only
        .address_space:  global
        .offset:         40
        .size:           8
        .value_kind:     global_buffer
    .group_segment_fixed_size: 87040
    .kernarg_segment_align: 8
    .kernarg_segment_size: 48
    .language:       OpenCL C
    .language_version:
      - 2
      - 0
    .max_flat_workgroup_size: 768
    .name:           _Z11attn_kernelPKiPKDv8_DF16_PKDF16_S5_PDF16_Pf
    .private_segment_fixed_size: 0
    .sgpr_count:     55
    .sgpr_spill_count: 0
    .symbol:         _Z11attn_kernelPKiPKDv8_DF16_PKDF16_S5_PDF16_Pf.kd
    .uniform_work_group_size: 1
    .uses_dynamic_stack: false
    .vgpr_count:     168
    .vgpr_spill_count: 0
    .wavefront_size: 64
  - .agpr_count:     12
    .args:
      - .actual_access:  read_only
        .address_space:  global
        .offset:         0
        .size:           8
        .value_kind:     global_buffer
      - .actual_access:  read_only
        .address_space:  global
        .offset:         8
        .size:           8
        .value_kind:     global_buffer
      - .actual_access:  read_only
        .address_space:  global
        .offset:         16
        .size:           8
        .value_kind:     global_buffer
      - .actual_access:  read_only
        .address_space:  global
        .offset:         24
        .size:           8
        .value_kind:     global_buffer
      - .actual_access:  read_only
        .address_space:  global
        .offset:         32
        .size:           8
        .value_kind:     global_buffer
      - .actual_access:  read_only
        .address_space:  global
        .offset:         40
        .size:           8
        .value_kind:     global_buffer
      - .actual_access:  write_only
        .address_space:  global
        .offset:         48
        .size:           8
        .value_kind:     global_buffer
    .group_segment_fixed_size: 16192
    .kernarg_segment_align: 8
    .kernarg_segment_size: 56
    .language:       OpenCL C
    .language_version:
      - 2
      - 0
    .max_flat_workgroup_size: 256
    .name:           _Z10epi_kernelPKDF16_PKfS2_S2_S2_S2_Pf
    .private_segment_fixed_size: 0
    .sgpr_count:     38
    .sgpr_spill_count: 0
    .symbol:         _Z10epi_kernelPKDF16_PKfS2_S2_S2_S2_Pf.kd
    .uniform_work_group_size: 1
    .uses_dynamic_stack: false
    .vgpr_count:     140
    .vgpr_spill_count: 0
    .wavefront_size: 64
